# removed the workgroup barrier between an attention unit's epilogue and the next unit's prologue (no LDS data is live across it)
# baseline (speedup 1.0000x reference)
.Lattn_pb3:
	s_waitcnt lgkmcnt(6)
	v_mfma_f32_16x16x32_bf16 v[64:67], v[160:163], v[96:99], 0
	v_exp_f32_e32 v88, v88
	v_mfma_f32_16x16x32_bf16 v[68:71], v[160:163], v[112:115], 0
	v_exp_f32_e32 v92, v92
	ds_read_b128 v[234:237], v209 offset:55296
	s_add_u32 s8, s16, 0x3bc00380
	s_addc_u32 s9, s17, 0
	s_add_u32 s6, s15, 0x23a80000
	s_addc_u32 s7, s14, 0
	s_waitcnt lgkmcnt(6)
	v_mfma_f32_16x16x32_bf16 v[0:3], v[164:167], v[216:219], v[0:3]
	v_cvt_pk_bf16_f32 v242, v80, v81
	v_mfma_f32_16x16x32_bf16 v[4:7], v[164:167], v[238:241], v[4:7]
	v_exp_f32_e32 v89, v89
	ds_read_b128 v[160:163], v201 offset:4096
	s_waitcnt vmcnt(4)
	ds_write_b128 v225, v[136:139] offset:32768
	s_waitcnt lgkmcnt(7)
	v_mfma_f32_16x16x32_bf16 v[68:71], v[168:171], v[116:119], v[68:71]
	v_exp_f32_e32 v93, v93
	v_mfma_f32_16x16x32_bf16 v[64:67], v[168:171], v[100:103], v[64:67]
	v_cvt_pk_bf16_f32 v243, v82, v83
	ds_read_b128 v[164:167], v209 offset:57344
	ds_write_b128 v226, v[140:143] offset:32768
	s_waitcnt lgkmcnt(8)
	v_mfma_f32_16x16x32_bf16 v[12:15], v[172:175], v[238:241], v[12:15]
	v_exp_f32_e32 v90, v90
	v_mfma_f32_16x16x32_bf16 v[8:11], v[172:175], v[216:219], v[8:11]
	v_exp_f32_e32 v94, v94
	ds_read_b128 v[168:171], v202 offset:4096
	ds_write_b64 v227, v[148:149] offset:16384
	s_waitcnt lgkmcnt(9)
	v_mfma_f32_16x16x32_bf16 v[64:67], v[176:179], v[104:107], v[64:67]
	v_cvt_pk_bf16_f32 v204, v84, v85
	v_mfma_f32_16x16x32_bf16 v[68:71], v[176:179], v[120:123], v[68:71]
	v_exp_f32_e32 v91, v91
	ds_read_b128 v[172:175], v209 offset:59392
	ds_write_b64 v228, v[150:151] offset:16384
	s_waitcnt lgkmcnt(10)
	v_mfma_f32_16x16x32_bf16 v[16:19], v[180:183], v[216:219], v[16:19]
	v_exp_f32_e32 v95, v95
	v_mfma_f32_16x16x32_bf16 v[20:23], v[180:183], v[238:241], v[20:23]
	v_cvt_pk_bf16_f32 v205, v86, v87
	v_add_f32_e32 v220, v220, v88
	ds_read_b128 v[176:179], v203 offset:4096
	ds_write_b64 v229, v[144:145] offset:16384
	s_waitcnt lgkmcnt(11)
	v_mfma_f32_16x16x32_bf16 v[68:71], v[230:233], v[124:127], v[68:71]
	v_add_f32_e32 v221, v221, v92
	v_add_f32_e32 v220, v220, v89
	v_mfma_f32_16x16x32_bf16 v[64:67], v[230:233], v[108:111], v[64:67]
	v_add_f32_e32 v221, v221, v93
	v_cvt_pk_bf16_f32 v244, v88, v89
	ds_read_b128 v[180:183], v209 offset:61440
	ds_write_b64 v184, v[146:147] offset:16384
	s_waitcnt lgkmcnt(12)
	v_mfma_f32_16x16x32_bf16 v[28:31], v[234:237], v[238:241], v[28:31]
	v_cvt_pk_bf16_f32 v245, v90, v91
	v_cvt_pk_bf16_f32 v206, v92, v93
	v_mfma_f32_16x16x32_bf16 v[24:27], v[234:237], v[216:219], v[24:27]
	v_cvt_pk_bf16_f32 v207, v94, v95
	ds_read_b128 v[230:233], v246 offset:4096
	global_load_dwordx4 v[148:151], v198, s[8:9]
	s_waitcnt lgkmcnt(12)
	v_mfma_f32_16x16x32_bf16 v[72:75], v[160:163], v[96:99], 0
	v_add_f32_e32 v220, v220, v90
	v_add_f32_e32 v221, v221, v94
	v_mfma_f32_16x16x32_bf16 v[76:79], v[160:163], v[112:115], 0
	v_add_f32_e32 v220, v220, v91
	v_add_f32_e32 v221, v221, v95
	ds_read_b128 v[234:237], v209 offset:63488
	global_load_dwordx4 v[144:147], v199, s[8:9]
	s_waitcnt lgkmcnt(11)
	v_mfma_f32_16x16x32_bf16 v[32:35], v[164:167], v[216:219], v[32:35]
	v_add_f32_e32 v194, v194, v220
	v_add_f32_e32 v195, v195, v221
	v_mfma_f32_16x16x32_bf16 v[36:39], v[164:167], v[238:241], v[36:39]
	v_exp_f32_e32 v64, v64
	ds_read_b128 v[160:163], v201 offset:8192
	global_load_dwordx4 v[136:139], v196, s[6:7]
	s_waitcnt lgkmcnt(10)
	v_mfma_f32_16x16x32_bf16 v[76:79], v[168:171], v[116:119], v[76:79]
	v_exp_f32_e32 v68, v68
	v_mfma_f32_16x16x32_bf16 v[72:75], v[168:171], v[100:103], v[72:75]
	v_exp_f32_e32 v65, v65
	ds_read_b128 v[164:167], v210 offset:49152
	global_load_dwordx4 v[140:143], v197, s[6:7]
	s_waitcnt lgkmcnt(9)
	v_mfma_f32_16x16x32_bf16 v[44:47], v[172:175], v[238:241], v[44:47]
	v_exp_f32_e32 v69, v69
	v_mfma_f32_16x16x32_bf16 v[40:43], v[172:175], v[216:219], v[40:43]
	v_exp_f32_e32 v66, v66
	ds_read_b128 v[168:171], v202 offset:8192
	s_waitcnt lgkmcnt(8)
	v_mfma_f32_16x16x32_bf16 v[72:75], v[176:179], v[104:107], v[72:75]
	v_exp_f32_e32 v70, v70
	v_mfma_f32_16x16x32_bf16 v[76:79], v[176:179], v[120:123], v[76:79]
	v_exp_f32_e32 v67, v67
	ds_read_b128 v[172:175], v210 offset:51200
	s_waitcnt lgkmcnt(7)
	v_mfma_f32_16x16x32_bf16 v[48:51], v[180:183], v[216:219], v[48:51]
	v_exp_f32_e32 v71, v71
	v_mfma_f32_16x16x32_bf16 v[52:55], v[180:183], v[238:241], v[52:55]
	v_add_f32_e32 v220, v64, v65
	ds_read_b128 v[176:179], v203 offset:8192
	s_waitcnt lgkmcnt(6)
	v_mfma_f32_16x16x32_bf16 v[76:79], v[230:233], v[124:127], v[76:79]
	v_add_f32_e32 v221, v68, v69
	v_mfma_f32_16x16x32_bf16 v[72:75], v[230:233], v[108:111], v[72:75]
	v_add_f32_e32 v220, v220, v66
	ds_read_b128 v[180:183], v210 offset:53248
	s_waitcnt lgkmcnt(6)
	v_mfma_f32_16x16x32_bf16 v[60:63], v[234:237], v[238:241], v[60:63]
	v_add_f32_e32 v221, v221, v70
	v_add_f32_e32 v220, v220, v67
	v_mfma_f32_16x16x32_bf16 v[56:59], v[234:237], v[216:219], v[56:59]
	v_add_f32_e32 v221, v221, v71
	ds_read_b128 v[230:233], v246 offset:8192
	s_waitcnt lgkmcnt(6)
	v_mfma_f32_16x16x32_bf16 v[80:83], v[160:163], v[96:99], 0
	v_exp_f32_e32 v72, v72
	v_mfma_f32_16x16x32_bf16 v[84:87], v[160:163], v[112:115], 0
	v_exp_f32_e32 v76, v76
	ds_read_b128 v[234:237], v210 offset:55296
	s_waitcnt lgkmcnt(6)
	v_mfma_f32_16x16x32_bf16 v[0:3], v[164:167], v[242:245], v[0:3]
	v_exp_f32_e32 v73, v73
	v_mfma_f32_16x16x32_bf16 v[4:7], v[164:167], v[204:207], v[4:7]
	v_exp_f32_e32 v77, v77
	ds_read_b128 v[160:163], v201 offset:12288
	s_waitcnt lgkmcnt(6)
	v_mfma_f32_16x16x32_bf16 v[84:87], v[168:171], v[116:119], v[84:87]
	v_exp_f32_e32 v74, v74
	v_mfma_f32_16x16x32_bf16 v[80:83], v[168:171], v[100:103], v[80:83]
	v_exp_f32_e32 v78, v78
	ds_read_b128 v[164:167], v210 offset:57344
	s_waitcnt lgkmcnt(6)
	v_mfma_f32_16x16x32_bf16 v[12:15], v[172:175], v[204:207], v[12:15]
	v_exp_f32_e32 v75, v75
	v_mfma_f32_16x16x32_bf16 v[8:11], v[172:175], v[242:245], v[8:11]
	v_exp_f32_e32 v79, v79
	ds_read_b128 v[168:171], v202 offset:12288
	s_waitcnt lgkmcnt(6)
	v_mfma_f32_16x16x32_bf16 v[80:83], v[176:179], v[104:107], v[80:83]
	v_add_f32_e32 v220, v220, v72
	v_add_f32_e32 v221, v221, v76
	v_mfma_f32_16x16x32_bf16 v[84:87], v[176:179], v[120:123], v[84:87]
	v_add_f32_e32 v220, v220, v73
	ds_read_b128 v[172:175], v210 offset:59392
	s_add_u32 s10, s10, 0x200
	s_addc_u32 s11, s11, 0
	s_add_u32 s12, s12, 0x40000
	s_addc_u32 s13, s13, 0
	s_add_i32 s4, s4, 4
	s_cmpk_lt_u32 s4, 0x104
	s_cselect_b64 s[6:7], -1, 0
	s_and_b64 s[6:7], s[0:1], s[6:7]
	s_and_b64 vcc, exec, s[6:7]
	s_waitcnt lgkmcnt(6)
	v_mfma_f32_16x16x32_bf16 v[16:19], v[180:183], v[242:245], v[16:19]
	v_add_f32_e32 v221, v221, v77
	v_add_f32_e32 v220, v220, v74
	v_mfma_f32_16x16x32_bf16 v[20:23], v[180:183], v[204:207], v[20:23]
	v_add_f32_e32 v221, v221, v78
	ds_read_b128 v[176:179], v203 offset:12288
	s_waitcnt lgkmcnt(6)
	v_mfma_f32_16x16x32_bf16 v[84:87], v[230:233], v[124:127], v[84:87]
	v_add_f32_e32 v220, v220, v75
	v_add_f32_e32 v221, v221, v79
	v_mfma_f32_16x16x32_bf16 v[80:83], v[230:233], v[108:111], v[80:83]
	v_cvt_pk_bf16_f32 v216, v64, v65
	ds_read_b128 v[180:183], v210 offset:61440
	s_waitcnt lgkmcnt(6)
	v_mfma_f32_16x16x32_bf16 v[28:31], v[234:237], v[204:207], v[28:31]
	v_cvt_pk_bf16_f32 v217, v66, v67
	v_cvt_pk_bf16_f32 v238, v68, v69
	v_mfma_f32_16x16x32_bf16 v[24:27], v[234:237], v[242:245], v[24:27]
	v_cvt_pk_bf16_f32 v239, v70, v71
	ds_read_b128 v[230:233], v246 offset:12288
	s_waitcnt lgkmcnt(6)
	v_mfma_f32_16x16x32_bf16 v[88:91], v[160:163], v[96:99], 0
	v_exp_f32_e32 v80, v80
	v_mfma_f32_16x16x32_bf16 v[92:95], v[160:163], v[112:115], 0
	v_exp_f32_e32 v84, v84
	ds_read_b128 v[234:237], v210 offset:63488
	s_waitcnt lgkmcnt(6)
	v_mfma_f32_16x16x32_bf16 v[32:35], v[164:167], v[242:245], v[32:35]
	v_exp_f32_e32 v81, v81
	v_mfma_f32_16x16x32_bf16 v[36:39], v[164:167], v[204:207], v[36:39]
	v_exp_f32_e32 v85, v85
	s_waitcnt lgkmcnt(5)
	v_mfma_f32_16x16x32_bf16 v[92:95], v[168:171], v[116:119], v[92:95]
	v_exp_f32_e32 v82, v82
	v_mfma_f32_16x16x32_bf16 v[88:91], v[168:171], v[100:103], v[88:91]
	v_exp_f32_e32 v86, v86
	s_waitcnt lgkmcnt(4)
	v_mfma_f32_16x16x32_bf16 v[44:47], v[172:175], v[204:207], v[44:47]
	v_exp_f32_e32 v83, v83
	v_mfma_f32_16x16x32_bf16 v[40:43], v[172:175], v[242:245], v[40:43]
	v_exp_f32_e32 v87, v87
	s_waitcnt lgkmcnt(3)
	v_mfma_f32_16x16x32_bf16 v[88:91], v[176:179], v[104:107], v[88:91]
	v_add_f32_e32 v220, v220, v80
	v_add_f32_e32 v221, v221, v84
	v_mfma_f32_16x16x32_bf16 v[92:95], v[176:179], v[120:123], v[92:95]
	v_add_f32_e32 v220, v220, v81
	s_waitcnt lgkmcnt(0)
	s_barrier
	ds_read_b128 v[160:163], v201 offset:16384
	ds_read_b128 v[164:167], v209 offset:0
	ds_read_b128 v[168:171], v202 offset:16384
	ds_read_b128 v[172:175], v209 offset:2048
	v_mfma_f32_16x16x32_bf16 v[48:51], v[180:183], v[242:245], v[48:51]
	v_add_f32_e32 v221, v221, v85
	v_add_f32_e32 v220, v220, v82
	v_mfma_f32_16x16x32_bf16 v[52:55], v[180:183], v[204:207], v[52:55]
	v_add_f32_e32 v221, v221, v86
	ds_read_b128 v[176:179], v203 offset:16384
	v_mfma_f32_16x16x32_bf16 v[92:95], v[230:233], v[124:127], v[92:95]
	v_add_f32_e32 v220, v220, v83
	v_add_f32_e32 v221, v221, v87
	v_mfma_f32_16x16x32_bf16 v[88:91], v[230:233], v[108:111], v[88:91]
	v_cvt_pk_bf16_f32 v218, v72, v73
	ds_read_b128 v[180:183], v209 offset:4096
	v_mfma_f32_16x16x32_bf16 v[60:63], v[234:237], v[204:207], v[60:63]
	v_cvt_pk_bf16_f32 v219, v74, v75
	v_cvt_pk_bf16_f32 v240, v76, v77
	v_mfma_f32_16x16x32_bf16 v[56:59], v[234:237], v[242:245], v[56:59]
	v_cvt_pk_bf16_f32 v241, v78, v79
	ds_read_b128 v[230:233], v246 offset:16384
	s_cbranch_vccnz .LBB0_734
	s_setprio 0
	s_waitcnt vmcnt(0)
	s_nop 7
	s_nop 7
	ds_swizzle_b32 v64, v194 offset:swizzle(SWAP,16)
	s_waitcnt lgkmcnt(0)
	v_add_f32_e32 v194, v194, v64
	v_mov_b32_e32 v65, v194
	s_nop 1
	v_permlane32_swap_b32_e32 v194, v65
	v_add_f32_e32 v194, v194, v65
	s_nop 0
	v_rcp_f32_e32 v66, v194
	ds_swizzle_b32 v64, v195 offset:swizzle(SWAP,16)
	s_waitcnt lgkmcnt(0)
	v_add_f32_e32 v195, v195, v64
	v_mov_b32_e32 v65, v195
	s_nop 1
	v_permlane32_swap_b32_e32 v195, v65
	v_add_f32_e32 v195, v195, v65
	s_nop 0
	v_rcp_f32_e32 v67, v195
	v_readlane_b32 s100, v250, 8
	v_mbcnt_lo_u32_b32 v68, -1, 0
	v_mbcnt_hi_u32_b32 v68, -1, v68
	v_and_b32_e32 v69, 15, v68
	v_lshrrev_b32_e32 v70, 4, v68
	s_lshr_b32 s101, s100, 1
	v_add_u32_e32 v69, s101, v69
	v_lshlrev_b32_e32 v69, 12, v69
	v_and_b32_e32 v71, 1, v70
	v_lshlrev_b32_e32 v71, 5, v71
	v_and_b32_e32 v70, 2, v70
	v_lshl_add_u32 v71, v70, 3, v71
	v_add_u32_e32 v70, v69, v71
	v_add_u32_e32 v71, 0x10000, v70
	v_mul_f32_e32 v0, v0, v66
	v_mul_f32_e32 v1, v1, v66
	v_mul_f32_e32 v2, v2, v66
	v_mul_f32_e32 v3, v3, v66
	v_mul_f32_e32 v8, v8, v66
	v_mul_f32_e32 v9, v9, v66
	v_mul_f32_e32 v10, v10, v66
	v_mul_f32_e32 v11, v11, v66
	v_cvt_pk_bf16_f32 v72, v0, v1
	v_cvt_pk_bf16_f32 v73, v2, v3
	v_cvt_pk_bf16_f32 v74, v8, v9
	v_cvt_pk_bf16_f32 v75, v10, v11
	s_nop 1
	v_permlane16_swap_b32_e32 v72, v74
	v_permlane16_swap_b32_e32 v73, v75
	s_nop 1
	global_store_dwordx4 v70, v[72:75], s[58:59] offset:0
	v_mul_f32_e32 v16, v16, v66
	v_mul_f32_e32 v17, v17, v66
	v_mul_f32_e32 v18, v18, v66
	v_mul_f32_e32 v19, v19, v66
	v_mul_f32_e32 v24, v24, v66
	v_mul_f32_e32 v25, v25, v66
	v_mul_f32_e32 v26, v26, v66
	v_mul_f32_e32 v27, v27, v66
	v_cvt_pk_bf16_f32 v76, v16, v17
	v_cvt_pk_bf16_f32 v77, v18, v19
	v_cvt_pk_bf16_f32 v78, v24, v25
	v_cvt_pk_bf16_f32 v79, v26, v27
	s_nop 1
	v_permlane16_swap_b32_e32 v76, v78
	v_permlane16_swap_b32_e32 v77, v79
	s_nop 1
	global_store_dwordx4 v70, v[76:79], s[58:59] offset:64
	v_mul_f32_e32 v32, v32, v66
	v_mul_f32_e32 v33, v33, v66
	v_mul_f32_e32 v34, v34, v66
	v_mul_f32_e32 v35, v35, v66
	v_mul_f32_e32 v40, v40, v66
	v_mul_f32_e32 v41, v41, v66
	v_mul_f32_e32 v42, v42, v66
	v_mul_f32_e32 v43, v43, v66
	v_cvt_pk_bf16_f32 v80, v32, v33
	v_cvt_pk_bf16_f32 v81, v34, v35
	v_cvt_pk_bf16_f32 v82, v40, v41
	v_cvt_pk_bf16_f32 v83, v42, v43
	s_nop 1
	v_permlane16_swap_b32_e32 v80, v82
	v_permlane16_swap_b32_e32 v81, v83
	s_nop 1
	global_store_dwordx4 v70, v[80:83], s[58:59] offset:128
	v_mul_f32_e32 v48, v48, v66
	v_mul_f32_e32 v49, v49, v66
	v_mul_f32_e32 v50, v50, v66
	v_mul_f32_e32 v51, v51, v66
	v_mul_f32_e32 v56, v56, v66
	v_mul_f32_e32 v57, v57, v66
	v_mul_f32_e32 v58, v58, v66
	v_mul_f32_e32 v59, v59, v66
	v_cvt_pk_bf16_f32 v84, v48, v49
	v_cvt_pk_bf16_f32 v85, v50, v51
	v_cvt_pk_bf16_f32 v86, v56, v57
	v_cvt_pk_bf16_f32 v87, v58, v59
	s_nop 1
	v_permlane16_swap_b32_e32 v84, v86
	v_permlane16_swap_b32_e32 v85, v87
	s_nop 1
	global_store_dwordx4 v70, v[84:87], s[58:59] offset:192
	v_mul_f32_e32 v4, v4, v67
	v_mul_f32_e32 v5, v5, v67
	v_mul_f32_e32 v6, v6, v67
	v_mul_f32_e32 v7, v7, v67
	v_mul_f32_e32 v12, v12, v67
	v_mul_f32_e32 v13, v13, v67
	v_mul_f32_e32 v14, v14, v67
	v_mul_f32_e32 v15, v15, v67
	v_cvt_pk_bf16_f32 v88, v4, v5
	v_cvt_pk_bf16_f32 v89, v6, v7
	v_cvt_pk_bf16_f32 v90, v12, v13
	v_cvt_pk_bf16_f32 v91, v14, v15
	s_nop 1
	v_permlane16_swap_b32_e32 v88, v90
	v_permlane16_swap_b32_e32 v89, v91
	s_nop 1
	global_store_dwordx4 v71, v[88:91], s[58:59] offset:0
	v_mul_f32_e32 v20, v20, v67
	v_mul_f32_e32 v21, v21, v67
	v_mul_f32_e32 v22, v22, v67
	v_mul_f32_e32 v23, v23, v67
	v_mul_f32_e32 v28, v28, v67
	v_mul_f32_e32 v29, v29, v67
	v_mul_f32_e32 v30, v30, v67
	v_mul_f32_e32 v31, v31, v67
	v_cvt_pk_bf16_f32 v92, v20, v21
	v_cvt_pk_bf16_f32 v93, v22, v23
	v_cvt_pk_bf16_f32 v94, v28, v29
	v_cvt_pk_bf16_f32 v95, v30, v31
	s_nop 1
	v_permlane16_swap_b32_e32 v92, v94
	v_permlane16_swap_b32_e32 v93, v95
	s_nop 1
	global_store_dwordx4 v71, v[92:95], s[58:59] offset:64
	v_mul_f32_e32 v36, v36, v67
	v_mul_f32_e32 v37, v37, v67
	v_mul_f32_e32 v38, v38, v67
	v_mul_f32_e32 v39, v39, v67
	v_mul_f32_e32 v44, v44, v67
	v_mul_f32_e32 v45, v45, v67
	v_mul_f32_e32 v46, v46, v67
	v_mul_f32_e32 v47, v47, v67
	v_cvt_pk_bf16_f32 v72, v36, v37
	v_cvt_pk_bf16_f32 v73, v38, v39
	v_cvt_pk_bf16_f32 v74, v44, v45
	v_cvt_pk_bf16_f32 v75, v46, v47
	s_nop 1
	v_permlane16_swap_b32_e32 v72, v74
	v_permlane16_swap_b32_e32 v73, v75
	s_nop 1
	global_store_dwordx4 v71, v[72:75], s[58:59] offset:128
	v_mul_f32_e32 v52, v52, v67
	v_mul_f32_e32 v53, v53, v67
	v_mul_f32_e32 v54, v54, v67
	v_mul_f32_e32 v55, v55, v67
	v_mul_f32_e32 v60, v60, v67
	v_mul_f32_e32 v61, v61, v67
	v_mul_f32_e32 v62, v62, v67
	v_mul_f32_e32 v63, v63, v67
	v_cvt_pk_bf16_f32 v76, v52, v53
	v_cvt_pk_bf16_f32 v77, v54, v55
	v_cvt_pk_bf16_f32 v78, v60, v61
	v_cvt_pk_bf16_f32 v79, v62, v63
	s_nop 1
	v_permlane16_swap_b32_e32 v76, v78
	v_permlane16_swap_b32_e32 v77, v79
	s_nop 1
	global_store_dwordx4 v71, v[76:79], s[58:59] offset:192
